# baseline (speedup 1.0000x reference)
.Lq_wait:
	s_waitcnt vmcnt(2)
	v_cmp_eq_u32_e32 vcc, s44, v141
	v_cmp_eq_u32_e64 s[6:7], s44, v143
	s_waitcnt vmcnt(1)
	v_cmp_eq_u32_e64 s[8:9], s44, v145
	s_and_b64 s[6:7], vcc, s[6:7]
	v_cmp_eq_u32_e64 s[54:55], s44, v147
	s_and_b64 s[6:7], s[6:7], s[8:9]
	s_waitcnt vmcnt(0)
	v_cmp_eq_u32_e64 s[12:13], s44, v149
	s_and_b64 s[6:7], s[6:7], s[54:55]
	v_cmp_eq_u32_e64 s[14:15], s44, v151
	s_and_b64 s[6:7], s[6:7], s[12:13]
	s_and_b64 s[6:7], s[6:7], s[14:15]
	s_cmp_eq_u64 s[6:7], exec
	s_cbranch_scc1 .LBB1_47
	s_add_i32 s45, s45, 1
	s_and_b32 s6, s45, 0x3ff
	s_cmp_lg_u32 s6, 0
	s_cbranch_scc1 .LBB1_38
	s_cmp_lt_u32 s45, 0x80001
	s_cbranch_scc0 .Lp9_timeout
	global_load_dword v141, v167, s[22:23] offset:4 sc1
	s_waitcnt vmcnt(0)
	v_readfirstlane_b32 s6, v141
	s_cmp_eq_u32 s6, 0
	s_cbranch_scc1 .LBB1_38
.Lp9_timeout:
	s_mov_b64 s[6:7], 0
	s_branch .LBB1_45
.LBB1_44:
	s_mov_b64 s[10:11], -1
	v_mov_b64_e32 v[140:141], 0
	v_mov_b64_e32 v[142:143], 0
	v_mov_b64_e32 v[144:145], 0
	v_mov_b64_e32 v[148:149], 0
	v_mov_b64_e32 v[146:147], 0
	v_mov_b64_e32 v[150:151], 0
	s_branch .LBB1_47

	.amdhsa_kernel _Z11lstm_kernel2LP
		.amdhsa_group_segment_fixed_size 38152
		.amdhsa_private_segment_fixed_size 0
		.amdhsa_kernarg_size 336
		.amdhsa_user_sgpr_count 2
		.amdhsa_user_sgpr_dispatch_ptr 0
		.amdhsa_user_sgpr_queue_ptr 0
		.amdhsa_user_sgpr_kernarg_segment_ptr 1
		.amdhsa_user_sgpr_dispatch_id 0
		.amdhsa_user_sgpr_kernarg_preload_length 0
		.amdhsa_user_sgpr_kernarg_preload_offset 0
		.amdhsa_user_sgpr_private_segment_size 0
		.amdhsa_uses_dynamic_stack 0
		.amdhsa_enable_private_segment 0
		.amdhsa_system_sgpr_workgroup_id_x 1
		.amdhsa_system_sgpr_workgroup_id_y 0
		.amdhsa_system_sgpr_workgroup_id_z 0
		.amdhsa_system_sgpr_workgroup_info 0
		.amdhsa_system_vgpr_workitem_id 2
		.amdhsa_next_free_vgpr 248
		.amdhsa_next_free_sgpr 56
		.amdhsa_accum_offset 248
		.amdhsa_reserve_vcc 1
		.amdhsa_float_round_mode_32 0
		.amdhsa_float_round_mode_16_64 0
		.amdhsa_float_denorm_mode_32 3
		.amdhsa_float_denorm_mode_16_64 3
		.amdhsa_dx10_clamp 1
		.amdhsa_ieee_mode 1
		.amdhsa_fp16_overflow 0
		.amdhsa_tg_split 0
		.amdhsa_exception_fp_ieee_invalid_op 0
		.amdhsa_exception_fp_denorm_src 0
		.amdhsa_exception_fp_ieee_div_zero 0
		.amdhsa_exception_fp_ieee_overflow 0
		.amdhsa_exception_fp_ieee_underflow 0
		.amdhsa_exception_fp_ieee_inexact 0
		.amdhsa_exception_int_div_zero 0
	.end_amdhsa_kernel

amdhsa.kernels:
  - .agpr_count:     0
    .args:
      - .actual_access:  read_only
        .address_space:  global
        .offset:         0
        .size:           8
        .value_kind:     global_buffer
      - .actual_access:  read_only
        .address_space:  global
        .offset:         8
        .size:           8
        .value_kind:     global_buffer
      - .actual_access:  read_only
        .address_space:  global
        .offset:         16
        .size:           8
        .value_kind:     global_buffer
      - .actual_access:  read_only
        .address_space:  global
        .offset:         24
        .size:           8
        .value_kind:     global_buffer
      - .actual_access:  read_only
        .address_space:  global
        .offset:         32
        .size:           8
        .value_kind:     global_buffer
      - .actual_access:  read_only
        .address_space:  global
        .offset:         40
        .size:           8
        .value_kind:     global_buffer
      - .actual_access:  read_only
        .address_space:  global
        .offset:         48
        .size:           8
        .value_kind:     global_buffer
      - .actual_access:  read_only
        .address_space:  global
        .offset:         56
        .size:           8
        .value_kind:     global_buffer
      - .actual_access:  write_only
        .address_space:  global
        .offset:         64
        .size:           8
        .value_kind:     global_buffer
      - .actual_access:  write_only
        .address_space:  global
        .offset:         72
        .size:           8
        .value_kind:     global_buffer
      - .offset:         80
        .size:           4
        .value_kind:     by_value
      - .actual_access:  read_only
        .address_space:  global
        .offset:         88
        .size:           8
        .value_kind:     global_buffer
      - .actual_access:  read_only
        .address_space:  global
        .offset:         96
        .size:           8
        .value_kind:     global_buffer
    .group_segment_fixed_size: 147456
    .kernarg_segment_align: 8
    .kernarg_segment_size: 104
    .language:       OpenCL C
    .language_version:
      - 2
      - 0
    .max_flat_workgroup_size: 512
    .name:           _Z13xg_gemm_f16x3PKiPKfS2_S2_S2_S2_S2_S2_PfPDv4_fiS2_S2_
    .private_segment_fixed_size: 0
    .sgpr_count:     36
    .sgpr_spill_count: 0
    .symbol:         _Z13xg_gemm_f16x3PKiPKfS2_S2_S2_S2_S2_S2_PfPDv4_fiS2_S2_.kd
    .uniform_work_group_size: 1
    .uses_dynamic_stack: false
    .vgpr_count:     242
    .vgpr_spill_count: 0
    .wavefront_size: 64
  - .agpr_count:     0
    .args:
      - .offset:         0
        .size:           80
        .value_kind:     by_value
      - .offset:         80
        .size:           4
        .value_kind:     hidden_block_count_x
      - .offset:         84
        .size:           4
        .value_kind:     hidden_block_count_y
      - .offset:         88
        .size:           4
        .value_kind:     hidden_block_count_z
      - .offset:         92
        .size:           2
        .value_kind:     hidden_group_size_x
      - .offset:         94
        .size:           2
        .value_kind:     hidden_group_size_y
      - .offset:         96
        .size:           2
        .value_kind:     hidden_group_size_z
      - .offset:         98
        .size:           2
        .value_kind:     hidden_remainder_x
      - .offset:         100
        .size:           2
        .value_kind:     hidden_remainder_y
      - .offset:         102
        .size:           2
        .value_kind:     hidden_remainder_z
      - .offset:         120
        .size:           8
        .value_kind:     hidden_global_offset_x
      - .offset:         128
        .size:           8
        .value_kind:     hidden_global_offset_y
      - .offset:         136
        .size:           8
        .value_kind:     hidden_global_offset_z
      - .offset:         144
        .size:           2
        .value_kind:     hidden_grid_dims
    .group_segment_fixed_size: 38152
    .kernarg_segment_align: 8
    .kernarg_segment_size: 336
    .language:       OpenCL C
    .language_version:
      - 2
      - 0
    .max_flat_workgroup_size: 512
    .name:           _Z11lstm_kernel2LP
    .private_segment_fixed_size: 0
    .sgpr_count:     62
    .sgpr_spill_count: 0
    .symbol:         _Z11lstm_kernel2LP.kd
    .uniform_work_group_size: 1
    .uses_dynamic_stack: false
    .vgpr_count:     248
    .vgpr_spill_count: 0
    .wavefront_size: 64
  - .agpr_count:     0
    .args:
      - .actual_access:  read_only
        .address_space:  global
        .offset:         0
        .size:           8
        .value_kind:     global_buffer
      - .actual_access:  read_only
        .address_space:  global
        .offset:         8
        .size:           8
        .value_kind:     global_buffer
      - .actual_access:  read_only
        .address_space:  global
        .offset:         16
        .size:           8
        .value_kind:     global_buffer
      - .actual_access:  write_only
        .address_space:  global
        .offset:         24
        .size:           8
        .value_kind:     global_buffer
    .group_segment_fixed_size: 0
    .kernarg_segment_align: 8
    .kernarg_segment_size: 32
    .language:       OpenCL C
    .language_version:
      - 2
      - 0
    .max_flat_workgroup_size: 256
    .name:           _Z12feats_kernelPKfS0_S0_Pd
    .private_segment_fixed_size: 0
    .sgpr_count:     14
    .sgpr_spill_count: 0
    .symbol:         _Z12feats_kernelPKfS0_S0_Pd.kd
    .uniform_work_group_size: 1
    .uses_dynamic_stack: false
    .vgpr_count:     116
    .vgpr_spill_count: 0
    .wavefront_size: 64
  - .agpr_count:     0
    .args:
      - .actual_access:  read_only
        .address_space:  global
        .offset:         0
        .size:           8
        .value_kind:     global_buffer
      - .actual_access:  read_only
        .address_space:  global
        .offset:         8
        .size:           8
        .value_kind:     global_buffer
      - .actual_access:  write_only
        .address_space:  global
        .offset:         16
        .size:           8
        .value_kind:     global_buffer
      - .actual_access:  write_only
        .address_space:  global
        .offset:         24
        .size:           8
        .value_kind:     global_buffer
    .group_segment_fixed_size: 19200
    .kernarg_segment_align: 8
    .kernarg_segment_size: 32
    .language:       OpenCL C
    .language_version:
      - 2
      - 0
    .max_flat_workgroup_size: 768
    .name:           _Z11vitA_kernelPKdPKfPdS3_
    .private_segment_fixed_size: 0
    .sgpr_count:     18
    .sgpr_spill_count: 0
    .symbol:         _Z11vitA_kernelPKdPKfPdS3_.kd
    .uniform_work_group_size: 1
    .uses_dynamic_stack: false
    .vgpr_count:     76
    .vgpr_spill_count: 0
    .wavefront_size: 64
  - .agpr_count:     0
    .args:
      - .actual_access:  read_only
        .address_space:  global
        .offset:         0
        .size:           8
        .value_kind:     global_buffer
      - .actual_access:  write_only
        .address_space:  global
        .offset:         8
        .size:           8
        .value_kind:     global_buffer
      - .actual_access:  write_only
        .address_space:  global
        .offset:         16
        .size:           8
        .value_kind:     global_buffer
      - .actual_access:  write_only
        .address_space:  global
        .offset:         24
        .size:           8
        .value_kind:     global_buffer
    .group_segment_fixed_size: 16128
    .kernarg_segment_align: 8
    .kernarg_segment_size: 32
    .language:       OpenCL C
    .language_version:
      - 2
      - 0
    .max_flat_workgroup_size: 576
    .name:           _Z12vitB1_kernelPKdPdS1_S1_
    .private_segment_fixed_size: 0
    .sgpr_count:     18
    .sgpr_spill_count: 0
    .symbol:         _Z12vitB1_kernelPKdPdS1_S1_.kd
    .uniform_work_group_size: 1
    .uses_dynamic_stack: false
    .vgpr_count:     59
    .vgpr_spill_count: 0
    .wavefront_size: 64
  - .agpr_count:     0
    .args:
      - .actual_access:  read_only
        .address_space:  global
        .offset:         0
        .size:           8
        .value_kind:     global_buffer
      - .actual_access:  read_only
        .address_space:  global
        .offset:         8
        .size:           8
        .value_kind:     global_buffer
      - .actual_access:  read_only
        .address_space:  global
        .offset:         16
        .size:           8
        .value_kind:     global_buffer
      - .actual_access:  read_only
        .address_space:  global
        .offset:         24
        .size:           8
        .value_kind:     global_buffer
      - .actual_access:  write_only
        .address_space:  global
        .offset:         32
        .size:           8
        .value_kind:     global_buffer
    .group_segment_fixed_size: 16320
    .kernarg_segment_align: 8
    .kernarg_segment_size: 40
    .language:       OpenCL C
    .language_version:
      - 2
      - 0
    .max_flat_workgroup_size: 1024
    .name:           _Z12vitB2_kernelPKdS0_S0_S0_Pd
    .private_segment_fixed_size: 0
    .sgpr_count:     42
    .sgpr_spill_count: 0
    .symbol:         _Z12vitB2_kernelPKdS0_S0_S0_Pd.kd
    .uniform_work_group_size: 1
    .uses_dynamic_stack: false
    .vgpr_count:     58
    .vgpr_spill_count: 0
    .wavefront_size: 64
  - .agpr_count:     0
    .args:
      - .actual_access:  read_only
        .address_space:  global
        .offset:         0
        .size:           8
        .value_kind:     global_buffer
      - .actual_access:  read_only
        .address_space:  global
        .offset:         8
        .size:           8
        .value_kind:     global_buffer
      - .actual_access:  read_only
        .address_space:  global
        .offset:         16
        .size:           8
        .value_kind:     global_buffer
      - .actual_access:  read_only
        .address_space:  global
        .offset:         24
        .size:           8
        .value_kind:     global_buffer
      - .actual_access:  write_only
        .address_space:  global
        .offset:         32
        .size:           8
        .value_kind:     global_buffer
      - .actual_access:  write_only
        .address_space:  global
        .offset:         40
        .size:           8
        .value_kind:     global_buffer
      - .actual_access:  write_only
        .address_space:  global
        .offset:         48
        .size:           8
        .value_kind:     global_buffer
    .group_segment_fixed_size: 0
    .kernarg_segment_align: 8
    .kernarg_segment_size: 56
    .language:       OpenCL C
    .language_version:
      - 2
      - 0
    .max_flat_workgroup_size: 64
    .name:           _Z11vitC_kernelPKdPKfS0_S0_PhPdS3_
    .private_segment_fixed_size: 0
    .sgpr_count:     34
    .sgpr_spill_count: 0
    .symbol:         _Z11vitC_kernelPKdPKfS0_S0_PhPdS3_.kd
    .uniform_work_group_size: 1
    .uses_dynamic_stack: false
    .vgpr_count:     86
    .vgpr_spill_count: 0
    .wavefront_size: 64
  - .agpr_count:     0
    .args:
      - .actual_access:  read_only
        .address_space:  global
        .offset:         0
        .size:           8
        .value_kind:     global_buffer
      - .actual_access:  read_only
        .address_space:  global
        .offset:         8
        .size:           8
        .value_kind:     global_buffer
      - .actual_access:  read_only
        .address_space:  global
        .offset:         16
        .size:           8
        .value_kind:     global_buffer
      - .actual_access:  read_only
        .address_space:  global
        .offset:         24
        .size:           8
        .value_kind:     global_buffer
      - .actual_access:  write_only
        .address_space:  global
        .offset:         32
        .size:           8
        .value_kind:     global_buffer
    .group_segment_fixed_size: 30424
    .kernarg_segment_align: 8
    .kernarg_segment_size: 40
    .language:       OpenCL C
    .language_version:
      - 2
      - 0
    .max_flat_workgroup_size: 1024
    .name:           _Z11vitD_kernelPKhPKdPKfS0_Pf
    .private_segment_fixed_size: 0
    .sgpr_count:     46
    .sgpr_spill_count: 0
    .symbol:         _Z11vitD_kernelPKhPKdPKfS0_Pf.kd
    .uniform_work_group_size: 1
    .uses_dynamic_stack: false
    .vgpr_count:     28
    .vgpr_spill_count: 0
    .wavefront_size: 64
